# instruction selection: per-unit accumulator zeroing of the bf16 GEMMs with v_mov_b64 (315 pairs of v_mov_b32 merged)
# speedup vs baseline: 1.0012x; 1.0005x over previous
;     __device__ __forceinline__ bool next(int i, Unit& u) const { return ord.next(i, u); }
; #define PG8_STAGEB(bufoff, gbase) do { _Pragma("unroll") for (int _i = 0; _i < 2; ++_i) PG8_GL((const char*)(gbase) + voffB[_i], bufoff, _i); } while (0)
; #define PG8_STAGEA(bufoff, ubase, offs, h, kb) do { _Pragma("unroll") for (int _i = 0; _i < 2; ++_i) { \
;         if constexpr (P::GATHER) PG8_GL(S.A + (size_t)(kb) + (offs)[h][_i], bufoff, _i); \
;         else PG8_GL((const char*)(ubase) + (size_t)(h) * hstepA + (size_t)(kb) + voffA[_i], bufoff, _i); } } while (0)
;     __device__ __forceinline__ bool next(int i_, Unit& u) const { const bool r = ord.next(i_, u); if (r) mt.locate(u.pm, u.e, u.lt); return r; }
;     __device__ __forceinline__ bool next(int i_, Unit& u) const { const bool r = ord.next(i_, u); if (r) mt.locate(u.pm, u.e, u.lt); return r; }
; template <class P, bool ALIGN_EPI>
; __device__ __forceinline__ void gemm_phase(ldsp lds, ldsp tab, const P& S) {
;     ...
;     Unit cur, nxt; int ui = 0;
;     if (!S.next(0, cur)) return;
;     Acc acc;
;     if constexpr (!P::FP8) {
; #pragma unroll
;         for (int a = 0; a < 2; ++a)
; #pragma unroll
;             for (int b = 0; b < 2; ++b)
; #pragma unroll
;                 for (int m = 0; m < 4; ++m)
; #pragma unroll
;                     for (int n = 0; n < 2; ++n) acc[a][b][m][n] = (f32x4){0.f, 0.f, 0.f, 0.f}; }
;     bf16x8 At[4][2], B0[2][2], B1[2][2];
;     const int sc8 = 0x7F7F7F7F; (void)sc8;
;     const char* cA = S.a_tile(cur); const char* cB = S.b_tile(cur);
;     unsigned goc[2][2] = {{0u, 0u}, {0u, 0u}}, gon[2][2] = {{0u, 0u}, {0u, 0u}};
;     if constexpr (P::GATHER) S.a_offs(cur, goc, sR, sC);
;     S.prepare(cur, 0, tab);
;     PG8_STAGEB(PG8_SB(0, 0), cB); PG8_STAGEB(PG8_SB(0, 1), cB + hstepB); PG8_STAGEA(PG8_SA(0, 0), cA, goc, 0, 0); PG8_STAGEA(PG8_SA(0, 1), cA, goc, 1, 0);
.LBB0_846:
	s_ashr_i32 s17, s16, 31
	s_lshl_b64 s[18:19], s[16:17], 19
	s_add_u32 s18, s50, s18
	s_addc_u32 s19, s51, s19
	s_ashr_i32 s15, s14, 31
	s_lshl_b64 s[20:21], s[14:15], 19
	s_add_u32 s20, s52, s20
	v_mov_b32_e32 v4, 0
	s_addc_u32 s21, s53, s21
	s_mov_b32 s3, -2
	s_mov_b64 s[38:39], 0x40080
	v_mov_b32_e32 v5, v4
	v_mov_b64_e32 v[6:7], 0
	v_mov_b64_e32 v[8:9], 0
	v_mov_b64_e32 v[10:11], 0
	v_mov_b64_e32 v[20:21], 0
	v_mov_b64_e32 v[22:23], 0
	v_mov_b64_e32 v[24:25], 0
	v_mov_b64_e32 v[26:27], 0
	v_mov_b64_e32 v[36:37], 0
	v_mov_b64_e32 v[38:39], 0
	v_mov_b64_e32 v[40:41], 0
	v_mov_b64_e32 v[42:43], 0
	v_mov_b64_e32 v[52:53], 0
	v_mov_b64_e32 v[54:55], 0
	v_mov_b64_e32 v[56:57], 0
	v_mov_b64_e32 v[58:59], 0
	v_mov_b64_e32 v[12:13], 0
	v_mov_b64_e32 v[14:15], 0
	v_mov_b64_e32 v[16:17], 0
	v_mov_b64_e32 v[18:19], 0
	v_mov_b64_e32 v[28:29], 0
	v_mov_b64_e32 v[30:31], 0
	v_mov_b64_e32 v[32:33], 0
	v_mov_b64_e32 v[34:35], 0
	v_mov_b64_e32 v[44:45], 0
	v_mov_b64_e32 v[46:47], 0
	v_mov_b64_e32 v[48:49], 0
	v_mov_b64_e32 v[50:51], 0
	v_mov_b64_e32 v[60:61], 0
	v_mov_b64_e32 v[62:63], 0
	v_mov_b64_e32 v[64:65], 0
	v_mov_b64_e32 v[66:67], 0
	v_mov_b64_e32 v[80:81], 0
	v_mov_b64_e32 v[82:83], 0
	v_mov_b64_e32 v[88:89], 0
	v_mov_b64_e32 v[90:91], 0
	v_mov_b64_e32 v[108:109], 0
	v_mov_b64_e32 v[110:111], 0
	v_mov_b64_e32 v[112:113], 0
	v_mov_b64_e32 v[114:115], 0
	v_mov_b64_e32 v[132:133], 0
	v_mov_b64_e32 v[134:135], 0
	v_mov_b64_e32 v[136:137], 0
	v_mov_b64_e32 v[138:139], 0
	v_mov_b64_e32 v[156:157], 0
	v_mov_b64_e32 v[158:159], 0
	v_mov_b64_e32 v[160:161], 0
	v_mov_b64_e32 v[162:163], 0
	v_mov_b64_e32 v[96:97], 0
	v_mov_b64_e32 v[98:99], 0
	v_mov_b64_e32 v[104:105], 0
	v_mov_b64_e32 v[106:107], 0
	v_mov_b64_e32 v[120:121], 0
	v_mov_b64_e32 v[122:123], 0
	v_mov_b64_e32 v[124:125], 0
	v_mov_b64_e32 v[126:127], 0
	v_mov_b64_e32 v[144:145], 0
	v_mov_b64_e32 v[146:147], 0
	v_mov_b64_e32 v[148:149], 0
	v_mov_b64_e32 v[150:151], 0
	v_mov_b64_e32 v[168:169], 0
	v_mov_b64_e32 v[170:171], 0
	v_mov_b64_e32 v[176:177], 0
	v_mov_b64_e32 v[178:179], 0
	.p2alignl 6, 3212836864

;     __device__ __forceinline__ bool next(int i, Unit& u) const { return ord.next(i, u); }
; #define PG8_STAGEB(bufoff, gbase) do { _Pragma("unroll") for (int _i = 0; _i < 2; ++_i) PG8_GL((const char*)(gbase) + voffB[_i], bufoff, _i); } while (0)
; #define PG8_STAGEA(bufoff, ubase, offs, h, kb) do { _Pragma("unroll") for (int _i = 0; _i < 2; ++_i) { \
;         if constexpr (P::GATHER) PG8_GL(S.A + (size_t)(kb) + (offs)[h][_i], bufoff, _i); \
;         else PG8_GL((const char*)(ubase) + (size_t)(h) * hstepA + (size_t)(kb) + voffA[_i], bufoff, _i); } } while (0)
;     __device__ __forceinline__ bool next(int i_, Unit& u) const { const bool r = ord.next(i_, u); if (r) mt.locate(u.pm, u.e, u.lt); return r; }
;     __device__ __forceinline__ bool next(int i_, Unit& u) const { const bool r = ord.next(i_, u); if (r) mt.locate(u.pm, u.e, u.lt); return r; }
; template <class P, bool ALIGN_EPI>
; __device__ __forceinline__ void gemm_phase(ldsp lds, ldsp tab, const P& S) {
;     ...
;     Unit cur, nxt; int ui = 0;
;     if (!S.next(0, cur)) return;
;     Acc acc;
;     if constexpr (!P::FP8) {
; #pragma unroll
;         for (int a = 0; a < 2; ++a)
; #pragma unroll
;             for (int b = 0; b < 2; ++b)
; #pragma unroll
;                 for (int m = 0; m < 4; ++m)
; #pragma unroll
;                     for (int n = 0; n < 2; ++n) acc[a][b][m][n] = (f32x4){0.f, 0.f, 0.f, 0.f}; }
;     bf16x8 At[4][2], B0[2][2], B1[2][2];
;     const int sc8 = 0x7F7F7F7F; (void)sc8;
;     const char* cA = S.a_tile(cur); const char* cB = S.b_tile(cur);
;     unsigned goc[2][2] = {{0u, 0u}, {0u, 0u}}, gon[2][2] = {{0u, 0u}, {0u, 0u}};
;     if constexpr (P::GATHER) S.a_offs(cur, goc, sR, sC);
;     S.prepare(cur, 0, tab);
;     PG8_STAGEB(PG8_SB(0, 0), cB); PG8_STAGEB(PG8_SB(0, 1), cB + hstepB); PG8_STAGEA(PG8_SA(0, 0), cA, goc, 0, 0); PG8_STAGEA(PG8_SA(0, 1), cA, goc, 1, 0);
.LBB0_997:
	s_ashr_i32 s15, s14, 31
	s_lshl_b64 s[16:17], s[14:15], 20
	s_add_u32 s16, s53, s16
	s_addc_u32 s17, s54, s17
	s_ashr_i32 s13, s12, 31
	s_lshl_b64 s[18:19], s[12:13], 17
	s_add_u32 s18, s55, s18
	v_mov_b32_e32 v4, 0
	s_addc_u32 s19, s56, s19
	s_mov_b32 s13, 0
	s_mov_b64 s[30:31], -1
	s_mov_b64 s[38:39], 0
	v_mov_b32_e32 v5, v4
	v_mov_b64_e32 v[6:7], 0
	v_mov_b64_e32 v[8:9], 0
	v_mov_b64_e32 v[10:11], 0
	v_mov_b64_e32 v[20:21], 0
	v_mov_b64_e32 v[22:23], 0
	v_mov_b64_e32 v[24:25], 0
	v_mov_b64_e32 v[26:27], 0
	v_mov_b64_e32 v[36:37], 0
	v_mov_b64_e32 v[38:39], 0
	v_mov_b64_e32 v[40:41], 0
	v_mov_b64_e32 v[42:43], 0
	v_mov_b64_e32 v[52:53], 0
	v_mov_b64_e32 v[54:55], 0
	v_mov_b64_e32 v[56:57], 0
	v_mov_b64_e32 v[58:59], 0
	v_mov_b64_e32 v[12:13], 0
	v_mov_b64_e32 v[14:15], 0
	v_mov_b64_e32 v[16:17], 0
	v_mov_b64_e32 v[18:19], 0
	v_mov_b64_e32 v[28:29], 0
	v_mov_b64_e32 v[30:31], 0
	v_mov_b64_e32 v[32:33], 0
	v_mov_b64_e32 v[34:35], 0
	v_mov_b64_e32 v[44:45], 0
	v_mov_b64_e32 v[46:47], 0
	v_mov_b64_e32 v[48:49], 0
	v_mov_b64_e32 v[50:51], 0
	v_mov_b64_e32 v[60:61], 0
	v_mov_b64_e32 v[62:63], 0
	v_mov_b64_e32 v[64:65], 0
	v_mov_b64_e32 v[66:67], 0
	v_mov_b64_e32 v[68:69], 0
	v_mov_b64_e32 v[70:71], 0
	v_mov_b64_e32 v[72:73], 0
	v_mov_b64_e32 v[74:75], 0
	v_mov_b64_e32 v[84:85], 0
	v_mov_b64_e32 v[86:87], 0
	v_mov_b64_e32 v[88:89], 0
	v_mov_b64_e32 v[90:91], 0
	v_mov_b64_e32 v[100:101], 0
	v_mov_b64_e32 v[102:103], 0
	v_mov_b64_e32 v[104:105], 0
	v_mov_b64_e32 v[106:107], 0
	v_mov_b64_e32 v[116:117], 0
	v_mov_b64_e32 v[118:119], 0
	v_mov_b64_e32 v[120:121], 0
	v_mov_b64_e32 v[122:123], 0
	v_mov_b64_e32 v[76:77], 0
	v_mov_b64_e32 v[78:79], 0
	v_mov_b64_e32 v[80:81], 0
	v_mov_b64_e32 v[82:83], 0
	v_mov_b64_e32 v[92:93], 0
	v_mov_b64_e32 v[94:95], 0
	v_mov_b64_e32 v[96:97], 0
	v_mov_b64_e32 v[98:99], 0
	v_mov_b64_e32 v[108:109], 0
	v_mov_b64_e32 v[110:111], 0
	v_mov_b64_e32 v[112:113], 0
	v_mov_b64_e32 v[114:115], 0
	v_mov_b64_e32 v[124:125], 0
	v_mov_b64_e32 v[126:127], 0
	v_mov_b64_e32 v[128:129], 0
	v_mov_b64_e32 v[130:131], 0
	.p2alignl 6, 3212836864

;     __device__ __forceinline__ bool next(int i, Unit& u) const { return ord.next(i, u); }
; #define PG8_STAGEB(bufoff, gbase) do { _Pragma("unroll") for (int _i = 0; _i < 2; ++_i) PG8_GL((const char*)(gbase) + voffB[_i], bufoff, _i); } while (0)
; #define PG8_STAGEA(bufoff, ubase, offs, h, kb) do { _Pragma("unroll") for (int _i = 0; _i < 2; ++_i) { \
;         if constexpr (P::GATHER) PG8_GL(S.A + (size_t)(kb) + (offs)[h][_i], bufoff, _i); \
;         else PG8_GL((const char*)(ubase) + (size_t)(h) * hstepA + (size_t)(kb) + voffA[_i], bufoff, _i); } } while (0)
;     __device__ __forceinline__ bool next(int i_, Unit& u) const { const bool r = ord.next(i_, u); if (r) mt.locate(u.pm, u.e, u.lt); return r; }
;     __device__ __forceinline__ bool next(int i_, Unit& u) const { const bool r = ord.next(i_, u); if (r) mt.locate(u.pm, u.e, u.lt); return r; }
; template <class P, bool ALIGN_EPI>
; __device__ __forceinline__ void gemm_phase(ldsp lds, ldsp tab, const P& S) {
;     ...
;     Unit cur, nxt; int ui = 0;
;     if (!S.next(0, cur)) return;
;     Acc acc;
;     if constexpr (!P::FP8) {
; #pragma unroll
;         for (int a = 0; a < 2; ++a)
; #pragma unroll
;             for (int b = 0; b < 2; ++b)
; #pragma unroll
;                 for (int m = 0; m < 4; ++m)
; #pragma unroll
;                     for (int n = 0; n < 2; ++n) acc[a][b][m][n] = (f32x4){0.f, 0.f, 0.f, 0.f}; }
;     bf16x8 At[4][2], B0[2][2], B1[2][2];
;     const int sc8 = 0x7F7F7F7F; (void)sc8;
;     const char* cA = S.a_tile(cur); const char* cB = S.b_tile(cur);
;     unsigned goc[2][2] = {{0u, 0u}, {0u, 0u}}, gon[2][2] = {{0u, 0u}, {0u, 0u}};
;     if constexpr (P::GATHER) S.a_offs(cur, goc, sR, sC);
;     S.prepare(cur, 0, tab);
;     PG8_STAGEB(PG8_SB(0, 0), cB); PG8_STAGEB(PG8_SB(0, 1), cB + hstepB); PG8_STAGEA(PG8_SA(0, 0), cA, goc, 0, 0); PG8_STAGEA(PG8_SA(0, 1), cA, goc, 1, 0);
.LBB0_1031:
	s_ashr_i32 s19, s18, 31
	s_lshl_b64 s[22:23], s[18:19], 20
	s_add_u32 s22, s49, s22
	s_addc_u32 s23, s50, s23
	v_mov_b32_e32 v127, 0
	s_andn2_b64 vcc, exec, s[14:15]
	s_cbranch_vccnz .LBB0_1041
	v_mov_b32_e32 v4, 0
	s_mov_b32 s19, 0
	s_mov_b64 s[42:43], 0x80080
	v_mov_b32_e32 v5, v4
	v_mov_b64_e32 v[6:7], 0
	v_mov_b64_e32 v[8:9], 0
	v_mov_b64_e32 v[10:11], 0
	v_mov_b64_e32 v[20:21], 0
	v_mov_b64_e32 v[22:23], 0
	v_mov_b64_e32 v[24:25], 0
	v_mov_b64_e32 v[26:27], 0
	v_mov_b64_e32 v[36:37], 0
	v_mov_b64_e32 v[38:39], 0
	v_mov_b64_e32 v[40:41], 0
	v_mov_b64_e32 v[42:43], 0
	v_mov_b64_e32 v[52:53], 0
	v_mov_b64_e32 v[54:55], 0
	v_mov_b64_e32 v[56:57], 0
	v_mov_b64_e32 v[58:59], 0
	v_mov_b64_e32 v[12:13], 0
	v_mov_b64_e32 v[14:15], 0
	v_mov_b64_e32 v[16:17], 0
	v_mov_b64_e32 v[18:19], 0
	v_mov_b64_e32 v[28:29], 0
	v_mov_b64_e32 v[30:31], 0
	v_mov_b64_e32 v[32:33], 0
	v_mov_b64_e32 v[34:35], 0
	v_mov_b64_e32 v[44:45], 0
	v_mov_b64_e32 v[46:47], 0
	v_mov_b64_e32 v[48:49], 0
	v_mov_b64_e32 v[50:51], 0
	v_mov_b64_e32 v[60:61], 0
	v_mov_b64_e32 v[62:63], 0
	v_mov_b64_e32 v[64:65], 0
	v_mov_b64_e32 v[66:67], 0
	v_mov_b64_e32 v[68:69], 0
	v_mov_b64_e32 v[70:71], 0
	v_mov_b64_e32 v[72:73], 0
	v_mov_b64_e32 v[74:75], 0
	v_mov_b64_e32 v[84:85], 0
	v_mov_b64_e32 v[86:87], 0
	v_mov_b64_e32 v[88:89], 0
	v_mov_b64_e32 v[90:91], 0
	v_mov_b64_e32 v[100:101], 0
	v_mov_b64_e32 v[102:103], 0
	v_mov_b64_e32 v[104:105], 0
	v_mov_b64_e32 v[106:107], 0
	v_mov_b64_e32 v[116:117], 0
	v_mov_b64_e32 v[118:119], 0
	v_mov_b64_e32 v[120:121], 0
	v_mov_b64_e32 v[122:123], 0
	v_mov_b64_e32 v[76:77], 0
	v_mov_b64_e32 v[78:79], 0
	v_mov_b64_e32 v[80:81], 0
	v_mov_b64_e32 v[82:83], 0
	v_mov_b64_e32 v[92:93], 0
	v_mov_b64_e32 v[94:95], 0
	v_mov_b64_e32 v[96:97], 0
	v_mov_b64_e32 v[98:99], 0
	v_mov_b64_e32 v[108:109], 0
	v_mov_b64_e32 v[110:111], 0
	v_mov_b64_e32 v[112:113], 0
	v_mov_b64_e32 v[114:115], 0
	v_mov_b64_e32 v[128:129], 0
	v_mov_b64_e32 v[130:131], 0
	v_mov_b64_e32 v[124:125], 0
	v_mov_b64_e32 v[126:127], 0
	.p2alignl 6, 3212836864

;     __device__ __forceinline__ bool next(int i, Unit& u) const { return ord.next(i, u); }
; #define PG8_STAGEB(bufoff, gbase) do { _Pragma("unroll") for (int _i = 0; _i < 2; ++_i) PG8_GL((const char*)(gbase) + voffB[_i], bufoff, _i); } while (0)
; #define PG8_STAGEA(bufoff, ubase, offs, h, kb) do { _Pragma("unroll") for (int _i = 0; _i < 2; ++_i) { \
;         if constexpr (P::GATHER) PG8_GL(S.A + (size_t)(kb) + (offs)[h][_i], bufoff, _i); \
;         else PG8_GL((const char*)(ubase) + (size_t)(h) * hstepA + (size_t)(kb) + voffA[_i], bufoff, _i); } } while (0)
;     __device__ __forceinline__ bool next(int i_, Unit& u) const { const bool r = ord.next(i_, u); if (r) mt.locate(u.pm, u.e, u.lt); return r; }
;     __device__ __forceinline__ bool next(int i_, Unit& u) const { const bool r = ord.next(i_, u); if (r) mt.locate(u.pm, u.e, u.lt); return r; }
; template <class P, bool ALIGN_EPI>
; __device__ __forceinline__ void gemm_phase(ldsp lds, ldsp tab, const P& S) {
;     ...
;     Unit cur, nxt; int ui = 0;
;     if (!S.next(0, cur)) return;
;     Acc acc;
;     if constexpr (!P::FP8) {
; #pragma unroll
;         for (int a = 0; a < 2; ++a)
; #pragma unroll
;             for (int b = 0; b < 2; ++b)
; #pragma unroll
;                 for (int m = 0; m < 4; ++m)
; #pragma unroll
;                     for (int n = 0; n < 2; ++n) acc[a][b][m][n] = (f32x4){0.f, 0.f, 0.f, 0.f}; }
;     bf16x8 At[4][2], B0[2][2], B1[2][2];
;     const int sc8 = 0x7F7F7F7F; (void)sc8;
;     const char* cA = S.a_tile(cur); const char* cB = S.b_tile(cur);
;     unsigned goc[2][2] = {{0u, 0u}, {0u, 0u}}, gon[2][2] = {{0u, 0u}, {0u, 0u}};
;     if constexpr (P::GATHER) S.a_offs(cur, goc, sR, sC);
;     S.prepare(cur, 0, tab);
;     PG8_STAGEB(PG8_SB(0, 0), cB); PG8_STAGEB(PG8_SB(0, 1), cB + hstepB); PG8_STAGEA(PG8_SA(0, 0), cA, goc, 0, 0); PG8_STAGEA(PG8_SA(0, 1), cA, goc, 1, 0);
.LBB0_1919:
	s_ashr_i32 s15, s14, 31
	s_lshl_b64 s[16:17], s[14:15], 19
	s_add_u32 s16, s42, s16
	s_addc_u32 s17, s43, s17
	s_ashr_i32 s13, s12, 31
	s_lshl_b64 s[18:19], s[12:13], 19
	s_add_u32 s18, s8, s18
	v_mov_b32_e32 v4, 0
	s_addc_u32 s19, s44, s19
	s_mov_b32 s13, -2
	s_mov_b64 s[30:31], 0x40080
	v_mov_b32_e32 v5, v4
	v_mov_b64_e32 v[6:7], 0
	v_mov_b64_e32 v[8:9], 0
	v_mov_b64_e32 v[10:11], 0
	v_mov_b64_e32 v[20:21], 0
	v_mov_b64_e32 v[22:23], 0
	v_mov_b64_e32 v[24:25], 0
	v_mov_b64_e32 v[26:27], 0
	v_mov_b64_e32 v[36:37], 0
	v_mov_b64_e32 v[38:39], 0
	v_mov_b64_e32 v[40:41], 0
	v_mov_b64_e32 v[42:43], 0
	v_mov_b64_e32 v[52:53], 0
	v_mov_b64_e32 v[54:55], 0
	v_mov_b64_e32 v[56:57], 0
	v_mov_b64_e32 v[58:59], 0
	v_mov_b64_e32 v[12:13], 0
	v_mov_b64_e32 v[14:15], 0
	v_mov_b64_e32 v[16:17], 0
	v_mov_b64_e32 v[18:19], 0
	v_mov_b64_e32 v[28:29], 0
	v_mov_b64_e32 v[30:31], 0
	v_mov_b64_e32 v[32:33], 0
	v_mov_b64_e32 v[34:35], 0
	v_mov_b64_e32 v[44:45], 0
	v_mov_b64_e32 v[46:47], 0
	v_mov_b64_e32 v[48:49], 0
	v_mov_b64_e32 v[50:51], 0
	v_mov_b64_e32 v[60:61], 0
	v_mov_b64_e32 v[62:63], 0
	v_mov_b64_e32 v[64:65], 0
	v_mov_b64_e32 v[66:67], 0
	v_mov_b64_e32 v[68:69], 0
	v_mov_b64_e32 v[70:71], 0
	v_mov_b64_e32 v[72:73], 0
	v_mov_b64_e32 v[74:75], 0
	v_mov_b64_e32 v[84:85], 0
	v_mov_b64_e32 v[86:87], 0
	v_mov_b64_e32 v[88:89], 0
	v_mov_b64_e32 v[90:91], 0
	v_mov_b64_e32 v[100:101], 0
	v_mov_b64_e32 v[102:103], 0
	v_mov_b64_e32 v[104:105], 0
	v_mov_b64_e32 v[106:107], 0
	v_mov_b64_e32 v[116:117], 0
	v_mov_b64_e32 v[118:119], 0
	v_mov_b64_e32 v[120:121], 0
	v_mov_b64_e32 v[122:123], 0
	v_mov_b64_e32 v[76:77], 0
	v_mov_b64_e32 v[78:79], 0
	v_mov_b64_e32 v[80:81], 0
	v_mov_b64_e32 v[82:83], 0
	v_mov_b64_e32 v[92:93], 0
	v_mov_b64_e32 v[94:95], 0
	v_mov_b64_e32 v[96:97], 0
	v_mov_b64_e32 v[98:99], 0
	v_mov_b64_e32 v[108:109], 0
	v_mov_b64_e32 v[110:111], 0
	v_mov_b64_e32 v[112:113], 0
	v_mov_b64_e32 v[114:115], 0
	v_mov_b64_e32 v[124:125], 0
	v_mov_b64_e32 v[126:127], 0
	v_mov_b64_e32 v[128:129], 0
	v_mov_b64_e32 v[130:131], 0
	.p2alignl 6, 3212836864

;     __device__ __forceinline__ bool next(int i, Unit& u) const { return ord.next(i, u); }
; #define PG8_STAGEB(bufoff, gbase) do { _Pragma("unroll") for (int _i = 0; _i < 2; ++_i) PG8_GL((const char*)(gbase) + voffB[_i], bufoff, _i); } while (0)
; #define PG8_STAGEA(bufoff, ubase, offs, h, kb) do { _Pragma("unroll") for (int _i = 0; _i < 2; ++_i) { \
;         if constexpr (P::GATHER) PG8_GL(S.A + (size_t)(kb) + (offs)[h][_i], bufoff, _i); \
;         else PG8_GL((const char*)(ubase) + (size_t)(h) * hstepA + (size_t)(kb) + voffA[_i], bufoff, _i); } } while (0)
;     __device__ __forceinline__ bool next(int i_, Unit& u) const { const bool r = ord.next(i_, u); if (r) mt.locate(u.pm, u.e, u.lt); return r; }
;     __device__ __forceinline__ bool next(int i_, Unit& u) const { const bool r = ord.next(i_, u); if (r) mt.locate(u.pm, u.e, u.lt); return r; }
; template <class P, bool ALIGN_EPI>
; __device__ __forceinline__ void gemm_phase(ldsp lds, ldsp tab, const P& S) {
;     ...
;     Unit cur, nxt; int ui = 0;
;     if (!S.next(0, cur)) return;
;     Acc acc;
;     if constexpr (!P::FP8) {
; #pragma unroll
;         for (int a = 0; a < 2; ++a)
; #pragma unroll
;             for (int b = 0; b < 2; ++b)
; #pragma unroll
;                 for (int m = 0; m < 4; ++m)
; #pragma unroll
;                     for (int n = 0; n < 2; ++n) acc[a][b][m][n] = (f32x4){0.f, 0.f, 0.f, 0.f}; }
;     bf16x8 At[4][2], B0[2][2], B1[2][2];
;     const int sc8 = 0x7F7F7F7F; (void)sc8;
;     const char* cA = S.a_tile(cur); const char* cB = S.b_tile(cur);
;     unsigned goc[2][2] = {{0u, 0u}, {0u, 0u}}, gon[2][2] = {{0u, 0u}, {0u, 0u}};
;     if constexpr (P::GATHER) S.a_offs(cur, goc, sR, sC);
;     S.prepare(cur, 0, tab);
;     PG8_STAGEB(PG8_SB(0, 0), cB); PG8_STAGEB(PG8_SB(0, 1), cB + hstepB); PG8_STAGEA(PG8_SA(0, 0), cA, goc, 0, 0); PG8_STAGEA(PG8_SA(0, 1), cA, goc, 1, 0);
.LBB0_2006:
	v_mov_b32_e32 v4, 0
	s_mov_b32 s2, -2
	s_mov_b64 s[22:23], 0xa0080
	v_mov_b32_e32 v5, v4
	v_mov_b64_e32 v[6:7], 0
	v_mov_b64_e32 v[8:9], 0
	v_mov_b64_e32 v[10:11], 0
	v_mov_b64_e32 v[12:13], 0
	v_mov_b64_e32 v[14:15], 0
	v_mov_b64_e32 v[16:17], 0
	v_mov_b64_e32 v[18:19], 0
	v_mov_b64_e32 v[20:21], 0
	v_mov_b64_e32 v[22:23], 0
	v_mov_b64_e32 v[24:25], 0
	v_mov_b64_e32 v[26:27], 0
	v_mov_b64_e32 v[28:29], 0
	v_mov_b64_e32 v[30:31], 0
	v_mov_b64_e32 v[32:33], 0
	v_mov_b64_e32 v[34:35], 0
	v_mov_b64_e32 v[64:65], 0
	v_mov_b64_e32 v[66:67], 0
	v_mov_b64_e32 v[72:73], 0
	v_mov_b64_e32 v[74:75], 0
	v_mov_b64_e32 v[76:77], 0
	v_mov_b64_e32 v[78:79], 0
	v_mov_b64_e32 v[80:81], 0
	v_mov_b64_e32 v[82:83], 0
	v_mov_b64_e32 v[84:85], 0
	v_mov_b64_e32 v[86:87], 0
	v_mov_b64_e32 v[88:89], 0
	v_mov_b64_e32 v[90:91], 0
	v_mov_b64_e32 v[92:93], 0
	v_mov_b64_e32 v[94:95], 0
	v_mov_b64_e32 v[96:97], 0
	v_mov_b64_e32 v[98:99], 0
	v_mov_b64_e32 v[36:37], 0
	v_mov_b64_e32 v[38:39], 0
	v_mov_b64_e32 v[40:41], 0
	v_mov_b64_e32 v[42:43], 0
	v_mov_b64_e32 v[44:45], 0
	v_mov_b64_e32 v[46:47], 0
	v_mov_b64_e32 v[48:49], 0
	v_mov_b64_e32 v[50:51], 0
	v_mov_b64_e32 v[52:53], 0
	v_mov_b64_e32 v[54:55], 0
	v_mov_b64_e32 v[56:57], 0
	v_mov_b64_e32 v[58:59], 0
	v_mov_b64_e32 v[60:61], 0
	v_mov_b64_e32 v[62:63], 0
	v_mov_b64_e32 v[68:69], 0
	v_mov_b64_e32 v[70:71], 0
	v_mov_b64_e32 v[116:117], 0
	v_mov_b64_e32 v[118:119], 0
	v_mov_b64_e32 v[120:121], 0
	v_mov_b64_e32 v[122:123], 0
	v_mov_b64_e32 v[124:125], 0
	v_mov_b64_e32 v[126:127], 0
	v_mov_b64_e32 v[128:129], 0
	v_mov_b64_e32 v[130:131], 0
	v_mov_b64_e32 v[132:133], 0
	v_mov_b64_e32 v[134:135], 0
	v_mov_b64_e32 v[136:137], 0
	v_mov_b64_e32 v[138:139], 0
	v_mov_b64_e32 v[140:141], 0
	v_mov_b64_e32 v[142:143], 0
	v_mov_b64_e32 v[144:145], 0
	v_mov_b64_e32 v[146:147], 0
	.p2alignl 6, 3212836864
